# one static s_setprio 1 for waves 4-7 at kernel entry, every per-phase s_setprio flip in the GEMM loops deleted
# baseline (speedup 1.0000x reference)
.LBB0_2:
	s_bitcmp1_b32 s33, 8
	s_cbranch_scc0 .Lprio_done
	s_setprio 1
